# P9: first-level routing/residual loads of the next token pair prefetched one iteration ahead (v120-147), iteration no longer starts with load->wait->lookup->load chain
# baseline (speedup 1.0000x reference)
.LBB0_1393:
	s_cmp_lt_i32 s28, 10
	s_cselect_b64 s[2:3], -1, 0
	s_and_b64 s[0:1], s[2:3], s[0:1]
	s_andn2_b64 vcc, exec, s[0:1]
	s_cbranch_vccnz .LBB0_1399
	v_readlane_b32 s0, v255, 8
	s_lshl_b32 s0, s0, 3
	v_readlane_b32 s1, v255, 18
	s_add_i32 s2, s0, s1
	s_cmpk_gt_i32 s2, 0x3fff
	s_cbranch_scc1 .LBB0_1399
	v_mbcnt_lo_u32_b32 v0, -1, 0
	v_mbcnt_hi_u32_b32 v4, -1, v0
	v_and_b32_e32 v0, 64, v4
	v_add_u32_e32 v0, 64, v0
	v_xor_b32_e32 v1, 1, v4
	v_cmp_lt_i32_e32 vcc, v1, v0
	v_readlane_b32 s15, v255, 2
	s_lshl_b32 s33, s15, 3
	v_cndmask_b32_e32 v1, v4, v1, vcc
	v_lshlrev_b32_e32 v28, 2, v1
	v_xor_b32_e32 v1, 2, v4
	v_cmp_lt_i32_e32 vcc, v1, v0
	s_add_i32 s6, s2, s33
	s_ashr_i32 s7, s6, 31
	v_cndmask_b32_e32 v1, v4, v1, vcc
	v_lshlrev_b32_e32 v29, 2, v1
	v_xor_b32_e32 v1, 4, v4
	v_cmp_lt_i32_e32 vcc, v1, v0
	s_lshl_b32 s4, s15, 4
	s_lshl_b64 s[6:7], s[6:7], 12
	v_cndmask_b32_e32 v1, v4, v1, vcc
	v_lshlrev_b32_e32 v30, 2, v1
	v_xor_b32_e32 v1, 8, v4
	v_cmp_lt_i32_e32 vcc, v1, v0
	v_mov_b32_e32 v9, 0
	s_add_u32 s6, s58, s6
	v_cndmask_b32_e32 v1, v4, v1, vcc
	v_lshlrev_b32_e32 v31, 2, v1
	v_xor_b32_e32 v1, 16, v4
	v_cmp_lt_i32_e32 vcc, v1, v0
	s_addc_u32 s7, s59, s7
	s_ashr_i32 s5, s4, 31
	v_cndmask_b32_e32 v1, v4, v1, vcc
	v_lshlrev_b32_e32 v32, 2, v1
	v_xor_b32_e32 v1, 32, v4
	v_cmp_lt_i32_e32 vcc, v1, v0
	s_ashr_i32 s3, s2, 31
	s_mov_b64 s[0:1], 0x8800000
	v_cndmask_b32_e32 v0, v4, v1, vcc
	v_lshlrev_b32_e32 v33, 2, v0
	v_lshlrev_b32_e32 v0, 3, v4
	v_mov_b32_e32 v1, v9
	v_lshl_add_u64 v[2:3], s[90:91], 0, v[0:1]
	s_lshl_b64 s[8:9], s[4:5], 12
	s_lshl_b64 s[10:11], s[2:3], 12
	v_lshl_add_u64 v[12:13], v[2:3], 0, s[0:1]
	v_lshlrev_b32_e32 v2, 2, v4
	v_mov_b32_e32 v3, v9
	s_add_u32 s10, s58, s10
	v_lshl_add_u64 v[14:15], s[12:13], 0, v[2:3]
	s_addc_u32 s11, s59, s11
	s_lshl_b64 s[12:13], s[2:3], 11
	s_add_u32 s12, s90, s12
	s_addc_u32 s13, s91, s13
	v_lshl_add_u64 v[0:1], s[12:13], 0, v[0:1]
	v_lshl_add_u64 v[16:17], v[0:1], 0, s[0:1]
	v_readlane_b32 s0, v255, 8
	v_readlane_b32 s1, v255, 18
	s_lshl_b32 s0, s0, 5
	s_lshl_b32 s1, s1, 2
	v_lshlrev_b32_e32 v8, 4, v4
	s_add_i32 s0, s0, s1
	v_lshl_add_u64 v[10:11], s[56:57], 0, v[8:9]
	s_lshl_b64 s[12:13], s[4:5], 11
	s_or_b32 s14, s0, 3
	s_lshl_b32 s3, s15, 6
	s_add_i32 s5, 0, 0x20400
	v_mov_b32_e32 v34, 0x3727c5ac
	s_mov_b32 s38, 0xf800000
	v_mov_b32_e32 v35, 0x260
	global_load_dwordx4 v[200:203], v[10:11], off
	global_load_dwordx4 v[204:207], v[10:11], off offset:1024
	global_load_dwordx4 v[208:211], v[10:11], off offset:2048
	global_load_dwordx4 v[212:215], v[10:11], off offset:3072
	s_mov_b32 s64, s2
	s_mov_b32 s62, s14
	v_mov_b64_e32 v[152:153], v[16:17]
	s_add_i32 s84, s33, s64
	s_cmpk_lt_i32 s84, 0x4000
	s_cselect_b32 s66, s84, s64
	s_lshl_b32 s68, s66, 2
	s_ashr_i32 s67, s66, 31
	s_ashr_i32 s69, s68, 31
	s_lshl_b64 s[60:61], s[66:67], 11
	s_lshl_b64 s[66:67], s[68:69], 2
	s_add_u32 s72, s40, s66
	s_addc_u32 s73, s41, s67
	s_add_u32 s70, s44, s66
	s_addc_u32 s71, s45, s67
	s_add_u32 s66, s36, s66
	s_addc_u32 s67, s37, s67
	s_or_b32 s68, s68, 2
	s_ashr_i32 s69, s68, 31
	s_lshl_b64 s[68:69], s[68:69], 2
	s_add_u32 s68, s36, s68
	s_addc_u32 s69, s37, s69
	s_ashr_i32 s63, s62, 31
	global_load_dwordx4 v[120:123], v9, s[72:73]
	s_add_i32 s80, s62, -3
	s_lshl_b64 s[72:73], s[62:63], 2
	s_add_u32 s82, s44, s72
	s_addc_u32 s83, s45, s73
	s_add_u32 s76, s40, s72
	s_addc_u32 s77, s41, s73
	s_add_i32 s74, s62, -1
	s_ashr_i32 s75, s74, 31
	s_lshl_b64 s[74:75], s[74:75], 2
	s_add_u32 s86, s44, s74
	s_addc_u32 s87, s45, s75
	s_add_u32 s78, s40, s74
	s_addc_u32 s79, s41, s75
	global_load_dword v124, v9, s[76:77]
	global_load_dword v125, v9, s[78:79]
	s_add_i32 s76, s62, -2
	s_ashr_i32 s77, s76, 31
	s_lshl_b64 s[76:77], s[76:77], 2
	s_add_u32 s78, s44, s76
	s_addc_u32 s79, s45, s77
	s_add_u32 s88, s40, s76
	s_addc_u32 s89, s41, s77
	global_load_dword v126, v9, s[88:89]
	global_load_dword v127, v9, s[86:87]
	global_load_dword v128, v9, s[82:83]
	s_ashr_i32 s81, s80, 31
	s_lshl_b64 s[80:81], s[80:81], 2
	s_add_u32 s82, s44, s80
	s_addc_u32 s83, s45, s81
	s_add_u32 s86, s40, s80
	s_addc_u32 s87, s41, s81
	global_load_dword v129, v9, s[86:87]
	global_load_dword v130, v9, s[78:79]
	global_load_dword v131, v9, s[82:83]
	global_load_dwordx2 v[132:133], v[152:153], off offset:1536 nt
	global_load_dwordx2 v[134:135], v[152:153], off offset:1024 nt
	global_load_dwordx2 v[136:137], v[152:153], off offset:512 nt
	global_load_dwordx4 v[140:143], v9, s[70:71]
	s_add_u32 s70, s36, s72
	s_addc_u32 s71, s37, s73
	s_add_u32 s72, s36, s74
	s_addc_u32 s73, s37, s75
	global_load_dword v144, v9, s[70:71]
	s_add_u32 s70, s36, s76
	s_addc_u32 s71, s37, s77
	s_add_u32 s74, s36, s80
	s_addc_u32 s75, s37, s81
	global_load_dword v145, v9, s[72:73]
	global_load_dword v146, v9, s[70:71]
	global_load_dword v147, v9, s[74:75]
	s_waitcnt vmcnt(0)
	s_branch .LBB0_1397

.LBB0_1397:
	s_add_i32 s39, s33, s2
	s_cmpk_lt_i32 s39, 0x4000
	s_cselect_b32 s16, s39, s2
	s_lshl_b32 s18, s16, 2
	s_ashr_i32 s17, s16, 31
	s_ashr_i32 s19, s18, 31
	s_lshl_b64 s[0:1], s[16:17], 11
	s_lshl_b64 s[16:17], s[18:19], 2
	s_add_u32 s22, s40, s16
	s_addc_u32 s23, s41, s17
	s_add_u32 s20, s44, s16
	s_addc_u32 s21, s45, s17
	s_add_u32 s16, s36, s16
	s_addc_u32 s17, s37, s17
	s_or_b32 s18, s18, 2
	s_ashr_i32 s19, s18, 31
	s_lshl_b64 s[18:19], s[18:19], 2
	s_add_u32 s18, s36, s18
	s_addc_u32 s19, s37, s19
	s_ashr_i32 s15, s14, 31
	s_add_i32 s30, s14, -3
	s_lshl_b64 s[22:23], s[14:15], 2
	s_add_u32 s34, s44, s22
	s_addc_u32 s35, s45, s23
	s_add_u32 s26, s40, s22
	s_addc_u32 s27, s41, s23
	s_add_i32 s24, s14, -1
	s_ashr_i32 s25, s24, 31
	s_lshl_b64 s[24:25], s[24:25], 2
	s_add_u32 s42, s44, s24
	s_addc_u32 s43, s45, s25
	s_add_u32 s28, s40, s24
	s_addc_u32 s29, s41, s25
	s_add_i32 s26, s14, -2
	s_ashr_i32 s27, s26, 31
	s_lshl_b64 s[26:27], s[26:27], 2
	s_add_u32 s28, s44, s26
	s_addc_u32 s29, s45, s27
	s_add_u32 s46, s40, s26
	s_addc_u32 s47, s41, s27
	s_ashr_i32 s31, s30, 31
	s_lshl_b64 s[30:31], s[30:31], 2
	s_add_u32 s34, s44, s30
	s_addc_u32 s35, s45, s31
	s_add_u32 s42, s40, s30
	s_addc_u32 s43, s41, s31
	s_add_u32 s20, s36, s22
	s_addc_u32 s21, s37, s23
	s_add_u32 s22, s36, s24
	s_addc_u32 s23, s37, s25
	s_add_u32 s20, s36, s26
	s_addc_u32 s21, s37, s27
	s_add_u32 s24, s36, s30
	s_addc_u32 s25, s37, s31
	s_cmpk_gt_i32 s39, 0x3fff
	s_waitcnt vmcnt(4)
	v_mov_b64_e32 v[0:1], v[120:121]
	v_mov_b64_e32 v[2:3], v[122:123]
	v_mov_b32_e32 v19, v124
	v_mov_b32_e32 v25, v125
	v_mov_b32_e32 v38, v126
	v_mov_b32_e32 v39, v127
	v_mov_b32_e32 v40, v128
	v_mov_b32_e32 v41, v129
	v_mov_b32_e32 v42, v130
	v_mov_b32_e32 v43, v131
	v_mov_b64_e32 v[26:27], v[132:133]
	v_mov_b64_e32 v[36:37], v[134:135]
	v_mov_b64_e32 v[20:21], v[136:137]
	v_mov_b64_e32 v[4:5], v[140:141]
	v_mov_b64_e32 v[6:7], v[142:143]
	v_mov_b32_e32 v18, v144
	v_mov_b32_e32 v24, v145
	v_mov_b32_e32 v22, v146
	v_mov_b32_e32 v23, v147
	v_lshlrev_b32_e32 v1, 2, v1
	v_lshlrev_b32_e32 v2, 2, v2
	v_lshlrev_b32_e32 v3, 2, v3
	v_add_u32_e32 v1, s5, v1
	v_add_u32_e32 v2, s5, v2
	v_add_u32_e32 v3, s5, v3
	v_lshlrev_b32_e32 v0, 2, v0
	v_add_u32_e32 v0, s5, v0
	v_lshlrev_b32_e32 v19, 2, v19
	v_lshlrev_b32_e32 v25, 2, v25
	v_add_u32_e32 v19, s5, v19
	v_add_u32_e32 v25, s5, v25
	v_lshlrev_b32_e32 v38, 2, v38
	v_add_u32_e32 v38, s5, v38
	ds_read_b32 v1, v1
	ds_read_b32 v25, v25
	ds_read_b32 v114, v2
	ds_read_b32 v115, v3
	ds_read_b32 v19, v19
	ds_read_b32 v44, v38
	s_waitcnt lgkmcnt(0)
	v_add_u32_e32 v2, v39, v25
	v_ashrrev_i32_e32 v3, 31, v2
	v_lshlrev_b64 v[2:3], 10, v[2:3]
	v_lshl_add_u64 v[38:39], v[14:15], 0, v[2:3]
	global_load_dword v60, v[38:39], off offset:768 nt
	global_load_dword v48, v[38:39], off nt
	global_load_dword v56, v[38:39], off offset:512 nt
	global_load_dword v52, v[38:39], off offset:256 nt
	global_load_dwordx2 v[2:3], v9, s[18:19]
	v_add_u32_e32 v38, v40, v19
	v_ashrrev_i32_e32 v39, 31, v38
	v_lshlrev_b64 v[38:39], 10, v[38:39]
	v_lshlrev_b32_e32 v19, 2, v41
	v_lshl_add_u64 v[38:39], v[14:15], 0, v[38:39]
	v_add_u32_e32 v19, s5, v19
	global_load_dword v64, v[38:39], off nt
	global_load_dword v68, v[38:39], off offset:256 nt
	global_load_dword v72, v[38:39], off offset:512 nt
	ds_read_b32 v19, v19
	v_add_u32_e32 v40, v42, v44
	v_ashrrev_i32_e32 v41, 31, v40
	v_lshlrev_b64 v[40:41], 10, v[40:41]
	v_lshl_add_u64 v[40:41], v[14:15], 0, v[40:41]
	s_waitcnt lgkmcnt(0)
	v_add_u32_e32 v42, v43, v19
	v_ashrrev_i32_e32 v43, 31, v42
	v_lshlrev_b64 v[42:43], 10, v[42:43]
	global_load_dword v74, v[40:41], off offset:768 nt
	v_lshl_add_u64 v[42:43], v[14:15], 0, v[42:43]
	global_load_dword v86, v[42:43], off nt
	global_load_dword v90, v[42:43], off offset:256 nt
	global_load_dword v94, v[42:43], off offset:512 nt
	global_load_dword v98, v[42:43], off offset:768 nt
	global_load_dword v102, v[40:41], off nt
	global_load_dword v106, v[40:41], off offset:256 nt
	global_load_dword v110, v[40:41], off offset:512 nt
	global_load_dword v116, v[38:39], off offset:768 nt
	global_load_dwordx2 v[44:45], v[16:17], off nt
	v_lshlrev_b32_e32 v40, 16, v36
	v_lshlrev_b32_e32 v119, 16, v20
	v_and_b32_e32 v20, 0xffff0000, v20
	v_lshlrev_b32_e32 v38, 16, v26
	v_lshlrev_b32_e32 v42, 16, v37
	v_mov_b32_e32 v25, v22
	v_and_b32_e32 v117, 0xffff0000, v36
	v_mov_b32_e32 v19, v24
	v_and_b32_e32 v39, 0xffff0000, v26
	v_lshlrev_b32_e32 v41, 16, v27
	v_and_b32_e32 v43, 0xffff0000, v27
	v_mov_b32_e32 v27, v22
	v_mov_b32_e32 v26, v23
	v_and_b32_e32 v118, 0xffff0000, v37
	v_mov_b32_e32 v37, v18
	v_mov_b32_e32 v36, v24
	s_waitcnt vmcnt(17)
	v_cvt_pk_f32_fp8_e32 v[58:59], v60
	s_waitcnt vmcnt(16)
	v_cvt_pk_f32_fp8_e32 v[46:47], v48
	s_waitcnt vmcnt(15)
	v_cvt_pk_f32_fp8_e32 v[54:55], v56
	s_waitcnt vmcnt(14)
	v_cvt_pk_f32_fp8_e32 v[50:51], v52
	v_cvt_pk_f32_fp8_sdwa v[52:53], v52 src0_sel:WORD_1
	v_mul_f32_e32 v75, v24, v59
	v_cvt_pk_f32_fp8_sdwa v[56:57], v56 src0_sel:WORD_1
	v_mov_b32_e32 v77, v51
	v_mov_b32_e32 v78, v52
	s_waitcnt vmcnt(12)
	v_cvt_pk_f32_fp8_e32 v[62:63], v64
	s_waitcnt vmcnt(11)
	v_cvt_pk_f32_fp8_e32 v[66:67], v68
	v_cvt_pk_f32_fp8_sdwa v[68:69], v68 src0_sel:WORD_1
	s_waitcnt vmcnt(10)
	v_cvt_pk_f32_fp8_e32 v[70:71], v72
	v_cvt_pk_f32_fp8_sdwa v[72:73], v72 src0_sel:WORD_1
	s_waitcnt vmcnt(8)
	v_cvt_pk_f32_fp8_e32 v[84:85], v86
	s_waitcnt vmcnt(7)
	v_cvt_pk_f32_fp8_e32 v[88:89], v90
	s_waitcnt vmcnt(6)
	v_cvt_pk_f32_fp8_e32 v[92:93], v94
	v_cvt_pk_f32_fp8_sdwa v[90:91], v90 src0_sel:WORD_1
	v_cvt_pk_f32_fp8_sdwa v[94:95], v94 src0_sel:WORD_1
	s_waitcnt vmcnt(3)
	v_cvt_pk_f32_fp8_e32 v[104:105], v106
	v_cvt_pk_f32_fp8_e32 v[80:81], v74
	s_waitcnt vmcnt(2)
	v_cvt_pk_f32_fp8_e32 v[108:109], v110
	v_cvt_pk_f32_fp8_e32 v[96:97], v98
	v_mov_b32_e32 v113, v88
	v_mov_b32_e32 v88, v105
	v_cvt_pk_f32_fp8_e32 v[100:101], v102
	v_cvt_pk_f32_fp8_sdwa v[106:107], v106 src0_sel:WORD_1
	v_cvt_pk_f32_fp8_sdwa v[110:111], v110 src0_sel:WORD_1
	v_pk_mul_f32 v[88:89], v[22:23], v[88:89]
	v_mov_b32_e32 v59, v80
	v_fmac_f32_e32 v40, v23, v92
	v_mov_b32_e32 v112, v104
	v_mov_b32_e32 v92, v109
	v_add_f32_e32 v20, v89, v20
	v_pk_mul_f32 v[58:59], v[24:25], v[58:59]
	v_fmac_f32_e32 v42, v23, v94
	v_fmac_f32_e32 v38, v23, v96
	v_mov_b32_e32 v104, v90
	v_mov_b32_e32 v90, v95
	v_pk_mul_f32 v[94:95], v[22:23], v[112:113]
	v_pk_mul_f32 v[92:93], v[22:23], v[92:93]
	v_add_f32_e32 v20, v88, v20
	s_waitcnt vmcnt(0)
	v_lshlrev_b32_e32 v88, 16, v44
	v_and_b32_e32 v89, 0xffff0000, v44
	v_mov_b32_e32 v44, v23
	v_mov_b32_e32 v79, v68
	v_mov_b32_e32 v68, v53
	v_mov_b32_e32 v52, v71
	v_mov_b32_e32 v53, v55
	v_cvt_pk_f32_fp8_sdwa v[86:87], v86 src0_sel:WORD_1
	v_cvt_pk_f32_fp8_sdwa v[98:99], v98 src0_sel:WORD_1
	v_add_f32_e32 v38, v59, v38
	v_add_f32_e32 v51, v95, v119
	v_add_f32_e32 v55, v93, v117
	v_pk_fma_f32 v[84:85], v[44:45], v[84:85], v[88:89] op_sel_hi:[0,1,1]
	v_cvt_pk_f32_fp8_sdwa v[82:83], v74 src0_sel:WORD_1
	v_pk_mul_f32 v[52:53], v[18:19], v[52:53]
	v_cvt_pk_f32_fp8_sdwa v[102:103], v102 src0_sel:WORD_1
	v_mov_b32_e32 v105, v106
	v_mov_b32_e32 v106, v91
	v_mov_b32_e32 v91, v111
	v_add_f32_e32 v59, v58, v38
	v_add_f32_e32 v38, v94, v51
	v_add_f32_e32 v51, v92, v55
	v_pk_fma_f32 v[84:85], v[22:23], v[100:101], v[84:85] op_sel_hi:[0,1,1]
	v_cvt_pk_f32_fp8_sdwa v[48:49], v48 src0_sel:WORD_1
	v_mov_b32_e32 v76, v67
	v_pk_mul_f32 v[104:105], v[26:27], v[104:105]
	v_pk_mul_f32 v[106:107], v[26:27], v[106:107]
	v_pk_mul_f32 v[26:27], v[26:27], v[90:91]
	v_add_f32_e32 v51, v53, v51
	v_pk_fma_f32 v[46:47], v[24:25], v[46:47], v[84:85] op_sel_hi:[0,1,1]
	v_cvt_pk_f32_fp8_sdwa v[60:61], v60 src0_sel:WORD_1
	v_pk_mul_f32 v[76:77], v[18:19], v[76:77]
	v_add_f32_e32 v26, v26, v118
	v_add_f32_e32 v80, v52, v51
	v_mov_b32_e32 v52, v57
	v_mov_b32_e32 v53, v73
	v_pk_fma_f32 v[62:63], v[18:19], v[62:63], v[46:47] op_sel_hi:[0,1,1]
	v_lshlrev_b32_e32 v46, 16, v45
	v_and_b32_e32 v47, 0xffff0000, v45
	v_pk_mul_f32 v[78:79], v[36:37], v[78:79]
	v_pk_mul_f32 v[68:69], v[36:37], v[68:69]
	v_add_f32_e32 v27, v26, v27
	v_add_f32_e32 v20, v77, v20
	v_pk_mul_f32 v[36:37], v[36:37], v[52:53]
	v_pk_fma_f32 v[44:45], v[44:45], v[86:87], v[46:47] op_sel_hi:[0,1,1]
	v_mov_b32_e32 v109, v98
	v_mov_b32_e32 v111, v99
	v_add_f32_e32 v26, v76, v20
	v_cvt_pk_f32_fp8_sdwa v[52:53], v116 src0_sel:WORD_1
	v_add_f32_e32 v20, v27, v36
	v_pk_fma_f32 v[44:45], v[22:23], v[102:103], v[44:45] op_sel_hi:[0,1,1]
	v_pk_fma_f32 v[40:41], v[22:23], v[108:109], v[40:41]
	v_pk_fma_f32 v[42:43], v[22:23], v[110:111], v[42:43]
	v_mov_b32_e32 v46, v24
	v_mov_b32_e32 v47, v23
	v_mov_b32_e32 v51, v97
	v_mov_b32_e32 v55, v82
	v_mov_b32_e32 v57, v83
	v_add_f32_e32 v90, v20, v37
	v_cvt_pk_f32_fp8_e32 v[36:37], v116
	v_pk_fma_f32 v[44:45], v[24:25], v[48:49], v[44:45] op_sel_hi:[0,1,1]
	v_pk_fma_f32 v[38:39], v[46:47], v[50:51], v[38:39]
	v_pk_fma_f32 v[40:41], v[24:25], v[54:55], v[40:41]
	v_pk_fma_f32 v[24:25], v[24:25], v[56:57], v[42:43]
	v_mov_b32_e32 v42, v18
	v_mov_b32_e32 v43, v22
	v_mov_b32_e32 v67, v81
	v_pk_fma_f32 v[54:55], v[42:43], v[66:67], v[38:39]
	v_mov_b32_e32 v71, v60
	v_pk_fma_f32 v[56:57], v[18:19], v[70:71], v[40:41]
	v_mov_b32_e32 v73, v61
	v_mov_b32_e32 v74, v54
	v_cvt_pk_f32_fp8_sdwa v[64:65], v64 src0_sel:WORD_1
	v_mul_f32_e32 v77, v18, v52
	v_pk_fma_f32 v[60:61], v[18:19], v[72:73], v[24:25]
	v_pk_mul_f32 v[22:23], v[54:55], v[54:55]
	v_pk_add_f32 v[24:25], v[54:55], v[74:75]
	v_mov_b32_e32 v76, v56
	v_mul_f32_e32 v53, v18, v53
	v_mul_f32_e32 v20, v80, v80
	v_mov_b32_e32 v23, v25
	v_mov_b32_e32 v27, v18
	v_mov_b32_e32 v38, v26
	v_mov_b32_e32 v39, v37
	v_pk_add_f32 v[48:49], v[56:57], v[76:77]
	v_mov_b32_e32 v52, v60
	v_mul_f32_e32 v58, v90, v90
	v_pk_fma_f32 v[66:67], v[26:27], v[38:39], v[22:23]
	v_pk_add_f32 v[70:71], v[60:61], v[52:53]
	v_pk_fma_f32 v[22:23], v[56:57], v[56:57], v[20:21]
	v_pk_mul_f32 v[38:39], v[48:49], v[48:49]
	v_pk_mul_f32 v[40:41], v[70:71], v[70:71]
	v_mov_b32_e32 v23, v39
	v_pk_fma_f32 v[38:39], v[60:61], v[60:61], v[58:59]
	v_pk_fma_f32 v[64:65], v[18:19], v[64:65], v[44:45] op_sel_hi:[0,1,1]
	v_mov_b32_e32 v39, v41
	v_pk_mul_f32 v[44:45], v[64:65], v[64:65]
	v_pk_add_f32 v[22:23], v[22:23], v[38:39]
	v_mov_b32_e32 v38, v62
	v_mov_b32_e32 v39, v18
	v_mov_b32_e32 v40, v62
	v_mov_b32_e32 v41, v36
	v_mul_f32_e32 v58, v63, v63
	v_mov_b32_e32 v42, v64
	v_mov_b32_e32 v43, v18
	v_mov_b32_e32 v46, v64
	v_mov_b32_e32 v47, v36
	v_pk_fma_f32 v[72:73], v[38:39], v[40:41], v[58:59]
	v_mov_b32_e32 v58, v45
	v_pk_fma_f32 v[38:39], v[42:43], v[46:47], v[58:59]
	v_lshlrev_b32_e32 v20, 16, v21
	v_pk_add_f32 v[40:41], v[72:73], v[38:39]
	v_pk_mul_f32 v[38:39], v[72:73], v[38:39]
	v_and_b32_e32 v21, 0xffff0000, v21
	v_mov_b32_e32 v41, v39
	v_mov_b32_e32 v38, v104
	v_mov_b32_e32 v39, v106
	v_pk_add_f32 v[20:21], v[38:39], v[20:21]
	v_mov_b32_e32 v106, v105
	v_pk_add_f32 v[20:21], v[20:21], v[106:107]
	v_mov_b32_e32 v38, v78
	v_mov_b32_e32 v39, v68
	v_pk_add_f32 v[20:21], v[20:21], v[38:39]
	v_mov_b32_e32 v68, v79
	v_pk_add_f32 v[58:59], v[20:21], v[68:69]
	v_lshl_add_u64 v[38:39], v[12:13], 0, s[0:1]
	v_pk_mul_f32 v[20:21], v[58:59], v[58:59]
	v_pk_mov_b32 v[18:19], v[58:59], v[18:19] op_sel:[1,0]
	v_mov_b32_e32 v36, v59
	v_mov_b32_e32 v21, v25
	v_pk_fma_f32 v[18:19], v[18:19], v[36:37], v[20:21]
	s_nop 0
	v_pk_add_f32 v[20:21], v[66:67], v[18:19]
	v_pk_mul_f32 v[18:19], v[66:67], v[18:19]
	s_nop 0
	v_mov_b32_e32 v21, v19
	v_pk_add_f32 v[18:19], v[40:41], v[20:21]
	s_nop 0
	v_pk_add_f32 v[18:19], v[18:19], v[22:23]
	ds_read_b32 v22, v0
	v_add_f32_e32 v18, v18, v19
	ds_bpermute_b32 v19, v28, v18
	v_add_u32_e32 v0, v5, v1
	v_ashrrev_i32_e32 v1, 31, v0
	s_waitcnt lgkmcnt(1)
	v_add_u32_e32 v4, v4, v22
	v_ashrrev_i32_e32 v5, 31, v4
	s_waitcnt lgkmcnt(0)
	v_add_f32_e32 v23, v18, v19
	global_load_dwordx2 v[20:21], v9, s[16:17]
	global_load_dwordx2 v[18:19], v9, s[16:17] offset:4
	ds_bpermute_b32 v24, v29, v23
	v_lshlrev_b64 v[36:37], 10, v[4:5]
	v_add_u32_e32 v4, v6, v114
	v_ashrrev_i32_e32 v5, 31, v4
	v_lshlrev_b64 v[68:69], 10, v[4:5]
	s_waitcnt lgkmcnt(0)
	v_add_f32_e32 v23, v23, v24
	ds_bpermute_b32 v27, v30, v23
	v_lshlrev_b64 v[24:25], 10, v[0:1]
	v_add_u32_e32 v0, v7, v115
	v_lshl_add_u64 v[36:37], v[14:15], 0, v[36:37]
	v_lshl_add_u64 v[24:25], v[14:15], 0, v[24:25]
	s_waitcnt lgkmcnt(0)
	v_add_f32_e32 v1, v23, v27
	ds_bpermute_b32 v22, v31, v1
	v_lshl_add_u64 v[68:69], v[14:15], 0, v[68:69]
	s_waitcnt lgkmcnt(0)
	v_add_f32_e32 v6, v1, v22
	ds_bpermute_b32 v7, v32, v6
	v_ashrrev_i32_e32 v1, 31, v0
	v_lshlrev_b64 v[40:41], 10, v[0:1]
	v_lshl_add_u64 v[74:75], v[14:15], 0, v[40:41]
	s_waitcnt lgkmcnt(0)
	v_add_f32_e32 v27, v6, v7
	ds_bpermute_b32 v42, v33, v27
	global_load_dwordx2 v[4:5], v[38:39], off nt
	global_load_dwordx2 v[0:1], v[38:39], off offset:512 nt
	global_load_dwordx2 v[6:7], v[38:39], off offset:1024 nt
	global_load_dwordx2 v[22:23], v[38:39], off offset:1536 nt
	s_waitcnt lgkmcnt(0)
	v_add_f32_e32 v27, v27, v42
	v_fmamk_f32 v27, v27, 0x3a800000, v34
	v_mul_f32_e32 v38, 0x4f800000, v27
	v_cmp_gt_f32_e32 vcc, s38, v27
	s_nop 1
	v_cndmask_b32_e32 v39, v27, v38, vcc
	v_sqrt_f32_e32 v42, v39
	global_load_dword v48, v[36:37], off nt
	global_load_dword v46, v[36:37], off offset:256 nt
	global_load_dword v47, v[36:37], off offset:512 nt
	global_load_dword v45, v[36:37], off offset:768 nt
	global_load_dword v44, v[24:25], off nt
	global_load_dword v43, v[24:25], off offset:256 nt
	global_load_dword v38, v[24:25], off offset:512 nt
	global_load_dword v27, v[24:25], off offset:768 nt
	v_add_u32_e32 v24, -1, v42
	v_fma_f32 v25, -v24, v42, v39
	v_cmp_ge_f32_e64 s[0:1], 0, v25
	v_add_u32_e32 v25, 1, v42
	v_fma_f32 v36, -v25, v42, v39
	v_cndmask_b32_e64 v24, v42, v24, s[0:1]
	v_cmp_lt_f32_e64 s[0:1], 0, v36
	s_nop 1
	v_cndmask_b32_e64 v24, v24, v25, s[0:1]
	v_mul_f32_e32 v25, 0x37800000, v24
	v_cndmask_b32_e32 v24, v24, v25, vcc
	v_cmp_class_f32_e32 vcc, v39, v35
	s_nop 1
	v_cndmask_b32_e32 v55, v24, v39, vcc
	v_div_scale_f32 v57, s[0:1], v55, v55, 1.0
	v_rcp_f32_e32 v61, v57
	global_load_dword v42, v[68:69], off nt
	global_load_dword v41, v[68:69], off offset:256 nt
	global_load_dword v40, v[68:69], off offset:512 nt
	global_load_dword v39, v[68:69], off offset:768 nt
	global_load_dword v36, v[74:75], off nt
	global_load_dword v37, v[74:75], off offset:256 nt
	global_load_dword v25, v[74:75], off offset:512 nt
	global_load_dword v24, v[74:75], off offset:768 nt
	s_add_i32 s64, s2, s4
	s_add_i32 s62, s14, s3
	s_cmpk_lt_i32 s64, 0x4000
	s_cselect_b32 s64, s64, s2
	s_cselect_b32 s62, s62, s14
	s_cselect_b64 s[92:93], s[12:13], 0
	v_lshl_add_u64 v[152:153], v[16:17], 0, s[92:93]
	s_add_i32 s84, s33, s64
	s_cmpk_lt_i32 s84, 0x4000
	s_cselect_b32 s66, s84, s64
	s_lshl_b32 s68, s66, 2
	s_ashr_i32 s67, s66, 31
	s_ashr_i32 s69, s68, 31
	s_lshl_b64 s[60:61], s[66:67], 11
	s_lshl_b64 s[66:67], s[68:69], 2
	s_add_u32 s72, s40, s66
	s_addc_u32 s73, s41, s67
	s_add_u32 s70, s44, s66
	s_addc_u32 s71, s45, s67
	s_add_u32 s66, s36, s66
	s_addc_u32 s67, s37, s67
	s_or_b32 s68, s68, 2
	s_ashr_i32 s69, s68, 31
	s_lshl_b64 s[68:69], s[68:69], 2
	s_add_u32 s68, s36, s68
	s_addc_u32 s69, s37, s69
	s_ashr_i32 s63, s62, 31
	global_load_dwordx4 v[120:123], v9, s[72:73]
	s_add_i32 s80, s62, -3
	s_lshl_b64 s[72:73], s[62:63], 2
	s_add_u32 s82, s44, s72
	s_addc_u32 s83, s45, s73
	s_add_u32 s76, s40, s72
	s_addc_u32 s77, s41, s73
	s_add_i32 s74, s62, -1
	s_ashr_i32 s75, s74, 31
	s_lshl_b64 s[74:75], s[74:75], 2
	s_add_u32 s86, s44, s74
	s_addc_u32 s87, s45, s75
	s_add_u32 s78, s40, s74
	s_addc_u32 s79, s41, s75
	global_load_dword v124, v9, s[76:77]
	global_load_dword v125, v9, s[78:79]
	s_add_i32 s76, s62, -2
	s_ashr_i32 s77, s76, 31
	s_lshl_b64 s[76:77], s[76:77], 2
	s_add_u32 s78, s44, s76
	s_addc_u32 s79, s45, s77
	s_add_u32 s88, s40, s76
	s_addc_u32 s89, s41, s77
	global_load_dword v126, v9, s[88:89]
	global_load_dword v127, v9, s[86:87]
	global_load_dword v128, v9, s[82:83]
	s_ashr_i32 s81, s80, 31
	s_lshl_b64 s[80:81], s[80:81], 2
	s_add_u32 s82, s44, s80
	s_addc_u32 s83, s45, s81
	s_add_u32 s86, s40, s80
	s_addc_u32 s87, s41, s81
	global_load_dword v129, v9, s[86:87]
	global_load_dword v130, v9, s[78:79]
	global_load_dword v131, v9, s[82:83]
	global_load_dwordx2 v[132:133], v[152:153], off offset:1536 nt
	global_load_dwordx2 v[134:135], v[152:153], off offset:1024 nt
	global_load_dwordx2 v[136:137], v[152:153], off offset:512 nt
	global_load_dwordx4 v[140:143], v9, s[70:71]
	s_add_u32 s70, s36, s72
	s_addc_u32 s71, s37, s73
	s_add_u32 s72, s36, s74
	s_addc_u32 s73, s37, s75
	global_load_dword v144, v9, s[70:71]
	s_add_u32 s70, s36, s76
	s_addc_u32 s71, s37, s77
	s_add_u32 s74, s36, s80
	s_addc_u32 s75, s37, s81
	global_load_dword v145, v9, s[72:73]
	global_load_dword v146, v9, s[70:71]
	global_load_dword v147, v9, s[74:75]
	s_cmpk_gt_i32 s39, 0x3fff
	v_lshl_add_u64 v[68:69], s[10:11], 0, v[8:9]
	v_fma_f32 v66, -v57, v61, 1.0
	v_fmac_f32_e32 v61, v66, v61
	v_div_scale_f32 v66, vcc, 1.0, v55, 1.0
	v_mul_f32_e32 v70, v66, v61
	v_fma_f32 v72, -v57, v70, v66
	v_fmac_f32_e32 v70, v72, v61
	v_fma_f32 v57, -v57, v70, v66
	v_div_fmas_f32 v57, v57, v61, v70
	v_div_fixup_f32 v72, v57, v55, 1.0
	v_pk_mul_f32 v[62:63], v[72:73], v[62:63] op_sel_hi:[0,1]
	v_pk_mul_f32 v[64:65], v[72:73], v[64:65] op_sel_hi:[0,1]
	v_mov_b32_e32 v55, v26
	v_pk_mul_f32 v[58:59], v[72:73], v[58:59] op_sel_hi:[0,1]
	v_pk_mul_f32 v[54:55], v[72:73], v[54:55] op_sel_hi:[0,1]
	v_mov_b32_e32 v57, v80
	v_mov_b32_e32 v61, v90
	s_waitcnt vmcnt(37)
	v_pk_mul_f32 v[52:53], v[202:203], v[64:65]
	v_pk_mul_f32 v[50:51], v[200:201], v[62:63]
	global_store_dwordx4 v[68:69], v[50:53], off
	v_pk_mul_f32 v[56:57], v[72:73], v[56:57] op_sel_hi:[0,1]
	v_mov_b32_e32 v70, v49
	v_mov_b32_e32 v66, v73
	v_pk_mul_f32 v[50:51], v[204:205], v[54:55]
	v_pk_mul_f32 v[52:53], v[206:207], v[58:59]
	global_store_dwordx4 v[68:69], v[50:53], off offset:1024
	v_pk_mul_f32 v[54:55], v[72:73], v[60:61] op_sel_hi:[0,1]
	s_nop 1
	v_pk_mul_f32 v[50:51], v[208:209], v[56:57]
	v_pk_mul_f32 v[52:53], v[210:211], v[54:55]
	global_store_dwordx4 v[68:69], v[50:53], off offset:2048
	v_pk_mul_f32 v[54:55], v[72:73], v[66:67] op_sel_hi:[0,1]
	v_pk_mul_f32 v[56:57], v[72:73], v[70:71] op_sel_hi:[0,1]
	v_pk_mul_f32 v[50:51], v[212:213], v[54:55]
	v_pk_mul_f32 v[52:53], v[214:215], v[56:57]
	global_store_dwordx4 v[68:69], v[50:53], off offset:3072
	s_waitcnt vmcnt(21)
	s_cbranch_scc1 .LBB0_1396
	s_nop 0
	v_and_b32_e32 v51, 0xffff0000, v23
	v_lshlrev_b32_e32 v53, 16, v23
	v_and_b32_e32 v49, 0xffff0000, v22
	v_lshlrev_b32_e32 v82, 16, v22
	v_cvt_pk_f32_fp8_e32 v[22:23], v46
	v_cvt_pk_f32_fp8_e32 v[66:67], v43
	v_mov_b32_e32 v70, v18
	v_mov_b32_e32 v71, v20
	v_mov_b32_e32 v73, v22
	v_mov_b32_e32 v72, v66
	v_and_b32_e32 v75, 0xffff0000, v0
	v_lshlrev_b32_e32 v0, 16, v0
	v_cvt_pk_f32_fp8_e32 v[56:57], v47
	v_cvt_pk_f32_fp8_sdwa v[58:59], v47 src0_sel:WORD_1
	v_cvt_pk_f32_fp8_sdwa v[46:47], v46 src0_sel:WORD_1
	v_cvt_pk_f32_fp8_sdwa v[68:69], v43 src0_sel:WORD_1
	v_pk_mul_f32 v[72:73], v[70:71], v[72:73]
	v_mov_b32_e32 v22, v67
	v_add_f32_e32 v0, v73, v0
	v_and_b32_e32 v26, 0xffff0000, v7
	v_lshlrev_b32_e32 v50, 16, v7
	v_and_b32_e32 v74, 0xffff0000, v6
	v_lshlrev_b32_e32 v52, 16, v6
	v_cvt_pk_f32_fp8_e32 v[6:7], v48
	v_cvt_pk_f32_fp8_sdwa v[54:55], v48 src0_sel:WORD_1
	v_add_f32_e32 v48, v72, v0
	v_pk_mul_f32 v[22:23], v[70:71], v[22:23]
	v_cvt_pk_f32_fp8_e32 v[72:73], v38
	v_add_f32_e32 v0, v23, v75
	v_add_f32_e32 v0, v22, v0
	v_mov_b32_e32 v22, v20
	v_mov_b32_e32 v23, v18
	v_mov_b32_e32 v67, v68
	v_mov_b32_e32 v68, v47
	v_cvt_pk_f32_fp8_e32 v[60:61], v45
	v_mov_b32_e32 v66, v46
	v_pk_mul_f32 v[46:47], v[22:23], v[68:69]
	v_cvt_pk_f32_fp8_sdwa v[68:69], v38 src0_sel:WORD_1
	v_fmac_f32_e32 v52, v20, v56
	v_mov_b32_e32 v56, v73
	v_pk_mul_f32 v[56:57], v[70:71], v[56:57]
	v_fmac_f32_e32 v82, v20, v60
	v_add_f32_e32 v38, v57, v74
	v_add_f32_e32 v60, v56, v38
	v_mov_b32_e32 v56, v59
	v_mov_b32_e32 v57, v69
	v_pk_mul_f32 v[66:67], v[22:23], v[66:67]
	v_pk_mul_f32 v[22:23], v[22:23], v[56:57]
	v_cvt_pk_f32_fp8_e32 v[56:57], v27
	v_cvt_pk_f32_fp8_e32 v[76:77], v39
	v_mov_b32_e32 v78, v2
	v_mov_b32_e32 v79, v18
	v_mov_b32_e32 v81, v56
	v_mov_b32_e32 v80, v76
	v_cvt_pk_f32_fp8_e32 v[70:71], v41
	v_pk_mul_f32 v[78:79], v[78:79], v[80:81]
	v_cvt_pk_f32_fp8_e32 v[80:81], v37
	v_add_f32_e32 v22, v22, v26
	v_add_f32_e32 v69, v22, v23
	v_cvt_pk_f32_fp8_sdwa v[22:23], v41 src0_sel:WORD_1
	v_add_f32_e32 v56, v79, v82
	v_cvt_pk_f32_fp8_e32 v[82:83], v36
	v_cvt_pk_f32_fp8_sdwa v[84:85], v36 src0_sel:WORD_1
	v_cvt_pk_f32_fp8_sdwa v[36:37], v37 src0_sel:WORD_1
	v_cvt_pk_f32_fp8_e32 v[74:75], v40
	v_cvt_pk_f32_fp8_e32 v[88:89], v25
	v_mov_b32_e32 v86, v81
	v_mov_b32_e32 v87, v71
	v_pk_mul_f32 v[86:87], v[2:3], v[86:87] op_sel:[1,0] op_sel_hi:[0,1]
	v_cvt_pk_f32_fp8_sdwa v[40:41], v40 src0_sel:WORD_1
	v_add_f32_e32 v0, v87, v0
	v_mov_b32_e32 v87, v22
	v_mov_b32_e32 v22, v37
	v_cvt_pk_f32_fp8_sdwa v[90:91], v25 src0_sel:WORD_1
	v_add_f32_e32 v79, v78, v56
	v_add_f32_e32 v56, v86, v0
	v_mov_b32_e32 v86, v36
	v_pk_mul_f32 v[36:37], v[2:3], v[22:23] op_sel:[1,0] op_sel_hi:[0,1]
	v_mov_b32_e32 v22, v89
	v_mov_b32_e32 v23, v75
	v_cvt_pk_f32_fp8_sdwa v[62:63], v45 src0_sel:WORD_1
	v_pk_mul_f32 v[22:23], v[2:3], v[22:23] op_sel:[1,0] op_sel_hi:[0,1]
	v_cvt_pk_f32_fp8_e32 v[64:65], v44
	v_cvt_pk_f32_fp8_sdwa v[44:45], v44 src0_sel:WORD_1
	v_cvt_pk_f32_fp8_sdwa v[26:27], v27 src0_sel:WORD_1
	v_add_f32_e32 v0, v23, v60
	v_add_f32_e32 v100, v22, v0
	v_mov_b32_e32 v22, v91
	v_mov_b32_e32 v23, v41
	v_pk_mul_f32 v[22:23], v[2:3], v[22:23] op_sel:[1,0] op_sel_hi:[0,1]
	v_lshlrev_b32_e32 v98, 16, v4
	v_and_b32_e32 v99, 0xffff0000, v4
	v_lshlrev_b32_e32 v4, 16, v5
	v_and_b32_e32 v5, 0xffff0000, v5
	v_fmac_f32_e32 v50, v20, v58
	v_add_f32_e32 v0, v69, v23
	v_pk_fma_f32 v[4:5], v[20:21], v[54:55], v[4:5] op_sel_hi:[0,1,1]
	v_mov_b32_e32 v73, v62
	v_mov_b32_e32 v69, v63
	v_cvt_pk_f32_fp8_sdwa v[38:39], v39 src0_sel:WORD_1
	v_pk_fma_f32 v[4:5], v[18:19], v[44:45], v[4:5] op_sel_hi:[0,1,1]
	v_pk_fma_f32 v[44:45], v[20:21], v[72:73], v[52:53] op_sel:[1,0,0] op_sel_hi:[0,1,1]
	v_pk_fma_f32 v[50:51], v[20:21], v[68:69], v[50:51] op_sel:[1,0,0] op_sel_hi:[0,1,1]
	v_mov_b32_e32 v52, v2
	v_mov_b32_e32 v53, v20
	v_mov_b32_e32 v71, v61
	v_mov_b32_e32 v41, v27
	v_cvt_pk_f32_fp8_sdwa v[92:93], v24 src0_sel:WORD_1
	v_cvt_pk_f32_fp8_e32 v[94:95], v24
	v_pk_fma_f32 v[6:7], v[20:21], v[6:7], v[98:99] op_sel_hi:[0,1,1]
	v_pk_fma_f32 v[20:21], v[52:53], v[70:71], v[48:49]
	v_mov_b32_e32 v75, v26
	v_pk_fma_f32 v[26:27], v[18:19], v[40:41], v[50:51] op_sel:[1,0,0] op_sel_hi:[0,1,1]
	v_mov_b32_e32 v40, v3
	v_mov_b32_e32 v41, v18
	v_mov_b32_e32 v81, v57
	v_pk_mul_f32 v[76:77], v[2:3], v[76:77] op_sel:[1,0] op_sel_hi:[0,1]
	v_pk_fma_f32 v[6:7], v[18:19], v[64:65], v[6:7] op_sel_hi:[0,1,1]
	v_pk_fma_f32 v[44:45], v[18:19], v[74:75], v[44:45] op_sel:[1,0,0] op_sel_hi:[0,1,1]
	v_pk_fma_f32 v[18:19], v[40:41], v[80:81], v[20:21]
	v_mov_b32_e32 v89, v38
	v_mov_b32_e32 v76, v18
	v_mov_b32_e32 v91, v39
	v_pk_mul_f32 v[38:39], v[18:19], v[18:19]
	v_pk_add_f32 v[40:41], v[18:19], v[76:77]
	v_cvt_pk_f32_fp8_e32 v[58:59], v42
	v_cvt_pk_f32_fp8_sdwa v[42:43], v42 src0_sel:WORD_1
	v_pk_mul_f32 v[96:97], v[2:3], v[92:93] op_sel:[1,0] op_sel_hi:[0,1]
	v_pk_fma_f32 v[20:21], v[2:3], v[88:89], v[44:45] op_sel:[1,0,0] op_sel_hi:[0,1,1]
	v_mov_b32_e32 v39, v41
	v_mov_b32_e32 v57, v3
	v_mov_b32_e32 v44, v56
	v_mov_b32_e32 v45, v95
	v_pk_mul_f32 v[92:93], v[2:3], v[92:93]
	v_pk_fma_f32 v[26:27], v[2:3], v[90:91], v[26:27] op_sel:[1,0,0] op_sel_hi:[0,1,1]
	v_pk_fma_f32 v[38:39], v[56:57], v[44:45], v[38:39]
	v_mov_b32_e32 v44, v20
	v_mov_b32_e32 v45, v96
	v_add_f32_e32 v101, v0, v22
	v_mul_f32_e32 v0, v100, v100
	v_pk_add_f32 v[44:45], v[20:21], v[44:45]
	v_mov_b32_e32 v92, v26
	v_mul_f32_e32 v60, v101, v101
	v_pk_add_f32 v[48:49], v[26:27], v[92:93]
	v_pk_fma_f32 v[50:51], v[20:21], v[20:21], v[0:1]
	v_pk_mul_f32 v[52:53], v[44:45], v[44:45]
	v_pk_fma_f32 v[6:7], v[2:3], v[58:59], v[6:7] op_sel_hi:[0,1,1]
	v_pk_fma_f32 v[4:5], v[2:3], v[42:43], v[4:5] op_sel_hi:[0,1,1]
	v_mov_b32_e32 v51, v53
	v_pk_fma_f32 v[52:53], v[26:27], v[26:27], v[60:61]
	v_pk_mul_f32 v[54:55], v[48:49], v[48:49]
	v_pk_fma_f32 v[6:7], v[2:3], v[82:83], v[6:7] op_sel:[1,0,0]
	v_pk_fma_f32 v[4:5], v[2:3], v[84:85], v[4:5] op_sel:[1,0,0]
	v_mov_b32_e32 v53, v55
	v_pk_mul_f32 v[86:87], v[2:3], v[86:87] op_sel:[1,0] op_sel_hi:[0,1]
	v_pk_mul_f32 v[42:43], v[4:5], v[4:5]
	v_pk_add_f32 v[50:51], v[50:51], v[52:53]
	v_mov_b32_e32 v2, v6
	v_mov_b32_e32 v52, v6
	v_mov_b32_e32 v53, v94
	v_mul_f32_e32 v78, v7, v7
	v_mov_b32_e32 v54, v4
	v_mov_b32_e32 v55, v3
	v_mov_b32_e32 v58, v4
	v_mov_b32_e32 v59, v94
	v_pk_fma_f32 v[52:53], v[2:3], v[52:53], v[78:79]
	v_mov_b32_e32 v78, v43
	v_pk_fma_f32 v[42:43], v[54:55], v[58:59], v[78:79]
	v_pk_add_f32 v[54:55], v[52:53], v[42:43]
	v_pk_mul_f32 v[42:43], v[52:53], v[42:43]
	v_lshlrev_b32_e32 v0, 16, v1
	v_mov_b32_e32 v55, v43
	v_and_b32_e32 v1, 0xffff0000, v1
	v_mov_b32_e32 v42, v66
	v_mov_b32_e32 v43, v46
	v_pk_add_f32 v[0:1], v[42:43], v[0:1]
	v_mov_b32_e32 v46, v67
	v_pk_add_f32 v[0:1], v[0:1], v[46:47]
	v_mov_b32_e32 v42, v87
	v_mov_b32_e32 v43, v37
	v_pk_add_f32 v[0:1], v[0:1], v[42:43]
	v_mov_b32_e32 v87, v36
	v_pk_add_f32 v[36:37], v[0:1], v[86:87]
	v_mov_b32_e32 v27, v101
	v_pk_mul_f32 v[0:1], v[36:37], v[36:37]
	v_mov_b32_e32 v2, v37
	v_mov_b32_e32 v94, v37
	v_mov_b32_e32 v1, v41
	v_pk_fma_f32 v[0:1], v[2:3], v[94:95], v[0:1]
	v_lshl_add_u64 v[40:41], s[6:7], 0, v[8:9]
	v_pk_add_f32 v[2:3], v[38:39], v[0:1]
	v_pk_mul_f32 v[0:1], v[38:39], v[0:1]
	v_mov_b32_e32 v48, v45
	v_mov_b32_e32 v3, v1
	v_pk_add_f32 v[0:1], v[54:55], v[2:3]
	v_mov_b32_e32 v38, v53
	v_pk_add_f32 v[0:1], v[0:1], v[50:51]
	s_nop 0
	v_add_f32_e32 v0, v0, v1
	ds_bpermute_b32 v1, v28, v0
	s_waitcnt lgkmcnt(0)
	v_add_f32_e32 v0, v0, v1
	ds_bpermute_b32 v1, v29, v0
	s_waitcnt lgkmcnt(0)
	v_add_f32_e32 v0, v0, v1
	ds_bpermute_b32 v1, v30, v0
	s_waitcnt lgkmcnt(0)
	v_add_f32_e32 v0, v0, v1
	ds_bpermute_b32 v1, v31, v0
	s_waitcnt lgkmcnt(0)
	v_add_f32_e32 v0, v0, v1
	ds_bpermute_b32 v1, v32, v0
	s_waitcnt lgkmcnt(0)
	v_add_f32_e32 v0, v0, v1
	ds_bpermute_b32 v1, v33, v0
	s_waitcnt lgkmcnt(0)
	v_add_f32_e32 v0, v0, v1
	v_fmamk_f32 v0, v0, 0x3a800000, v34
	v_mul_f32_e32 v1, 0x4f800000, v0
	v_cmp_gt_f32_e32 vcc, s38, v0
	s_nop 1
	v_cndmask_b32_e32 v0, v0, v1, vcc
	v_sqrt_f32_e32 v1, v0
	s_nop 0
	v_add_u32_e32 v2, -1, v1
	v_fma_f32 v3, -v2, v1, v0
	v_cmp_ge_f32_e64 s[0:1], 0, v3
	v_add_u32_e32 v3, 1, v1
	s_nop 0
	v_cndmask_b32_e64 v2, v1, v2, s[0:1]
	v_fma_f32 v1, -v3, v1, v0
	v_cmp_lt_f32_e64 s[0:1], 0, v1
	s_nop 1
	v_cndmask_b32_e64 v1, v2, v3, s[0:1]
	v_mul_f32_e32 v2, 0x37800000, v1
	v_cndmask_b32_e32 v1, v1, v2, vcc
	v_cmp_class_f32_e32 vcc, v0, v35
	s_nop 1
	v_cndmask_b32_e32 v0, v1, v0, vcc
	v_div_scale_f32 v1, s[0:1], v0, v0, 1.0
	v_rcp_f32_e32 v2, v1
	s_nop 0
	v_fma_f32 v3, -v1, v2, 1.0
	v_fmac_f32_e32 v2, v3, v2
	v_div_scale_f32 v3, vcc, 1.0, v0, 1.0
	v_mul_f32_e32 v19, v3, v2
	v_fma_f32 v21, -v1, v19, v3
	v_fmac_f32_e32 v19, v21, v2
	v_fma_f32 v1, -v1, v19, v3
	v_div_fmas_f32 v1, v1, v2, v19
	v_div_fixup_f32 v42, v1, v0, 1.0
	v_pk_mul_f32 v[0:1], v[42:43], v[6:7] op_sel_hi:[0,1]
	v_pk_mul_f32 v[2:3], v[42:43], v[4:5] op_sel_hi:[0,1]
	s_waitcnt vmcnt(21)
	v_pk_mul_f32 v[2:3], v[202:203], v[2:3]
	v_pk_mul_f32 v[0:1], v[200:201], v[0:1]
	global_store_dwordx4 v[40:41], v[0:3], off
	v_mov_b32_e32 v19, v56
	v_pk_mul_f32 v[4:5], v[42:43], v[36:37] op_sel_hi:[0,1]
	v_pk_mul_f32 v[6:7], v[42:43], v[18:19] op_sel_hi:[0,1]
	v_mov_b32_e32 v21, v100
	v_pk_mul_f32 v[0:1], v[204:205], v[6:7]
	v_pk_mul_f32 v[2:3], v[206:207], v[4:5]
	global_store_dwordx4 v[40:41], v[0:3], off offset:1024
	v_pk_mul_f32 v[4:5], v[42:43], v[26:27] op_sel_hi:[0,1]
	v_pk_mul_f32 v[6:7], v[42:43], v[20:21] op_sel_hi:[0,1]
	v_pk_mul_f32 v[0:1], v[208:209], v[6:7]
	v_pk_mul_f32 v[2:3], v[210:211], v[4:5]
	global_store_dwordx4 v[40:41], v[0:3], off offset:2048
	v_pk_mul_f32 v[4:5], v[42:43], v[38:39] op_sel_hi:[0,1]
	v_pk_mul_f32 v[6:7], v[42:43], v[48:49] op_sel_hi:[0,1]
	v_pk_mul_f32 v[0:1], v[212:213], v[4:5]
	v_pk_mul_f32 v[2:3], v[214:215], v[6:7]
	global_store_dwordx4 v[40:41], v[0:3], off offset:3072
	s_branch .LBB0_1396
